# mod_phase adaLN GEMV loop software-pipelined: 32 row loads in flight per wave (4 register sets, counted vmcnt), on top of v28
# baseline (speedup 1.0000x reference)
.LBB0_101:
	s_mul_hi_i32 s4, s17, 0x2aaaaaab
	s_lshr_b32 s5, s4, 31
	s_ashr_i32 s18, s4, 3
	s_add_i32 s18, s18, s5
	s_mul_i32 s4, s18, 48
	s_sub_i32 s19, s17, s4
	v_readlane_b32 s4, v254, 1
	v_readlane_b32 s5, v254, 2
	s_load_dwordx2 s[6:7], s[4:5], 0x78
	s_waitcnt lgkmcnt(0)
	s_lshl_b32 s4, s19, 6
	s_ashr_i32 s5, s4, 31
	s_mul_i32 s9, s18, 0xc00000
	s_mov_b64 s[20:21], s[6:7]
	s_lshl_b64 s[6:7], s[4:5], 2
	s_mul_hi_i32 s8, s18, 0xc00000
	s_add_u32 s6, s9, s6
	s_addc_u32 s7, s8, s7
	s_add_u32 s20, s20, s6
	s_addc_u32 s21, s21, s7
	s_mov_b64 s[22:23], s[20:21]
	s_mov_b32 s24, 0
	s_mov_b64 s[8:9], 0
	v_mov_b32_e32 v15, v13
	v_mov_b32_e32 v8, 0
	v_mov_b32_e32 v9, v1
	v_mov_b32_e32 v10, 0
	v_mov_b32_e32 v11, v1
	global_load_dword v48, v4, s[22:23]
	s_add_u32 s22, s22, 0x3000
	s_addc_u32 s23, s23, 0
	global_load_dword v50, v4, s[22:23]
	s_add_u32 s22, s22, 0x3000
	s_addc_u32 s23, s23, 0
	global_load_dword v52, v4, s[22:23]
	s_add_u32 s22, s22, 0x3000
	s_addc_u32 s23, s23, 0
	global_load_dword v54, v4, s[22:23]
	s_add_u32 s22, s22, 0x3000
	s_addc_u32 s23, s23, 0
	global_load_dword v56, v4, s[22:23]
	s_add_u32 s22, s22, 0x3000
	s_addc_u32 s23, s23, 0
	global_load_dword v58, v4, s[22:23]
	s_add_u32 s22, s22, 0x3000
	s_addc_u32 s23, s23, 0
	global_load_dword v60, v4, s[22:23]
	s_add_u32 s22, s22, 0x3000
	s_addc_u32 s23, s23, 0
	global_load_dword v62, v4, s[22:23]
	s_add_u32 s22, s22, 0x3000
	s_addc_u32 s23, s23, 0
	global_load_dword v72, v4, s[22:23]
	s_add_u32 s22, s22, 0x3000
	s_addc_u32 s23, s23, 0
	global_load_dword v74, v4, s[22:23]
	s_add_u32 s22, s22, 0x3000
	s_addc_u32 s23, s23, 0
	global_load_dword v76, v4, s[22:23]
	s_add_u32 s22, s22, 0x3000
	s_addc_u32 s23, s23, 0
	global_load_dword v78, v4, s[22:23]
	s_add_u32 s22, s22, 0x3000
	s_addc_u32 s23, s23, 0
	global_load_dword v80, v4, s[22:23]
	s_add_u32 s22, s22, 0x3000
	s_addc_u32 s23, s23, 0
	global_load_dword v82, v4, s[22:23]
	s_add_u32 s22, s22, 0x3000
	s_addc_u32 s23, s23, 0
	global_load_dword v84, v4, s[22:23]
	s_add_u32 s22, s22, 0x3000
	s_addc_u32 s23, s23, 0
	global_load_dword v86, v4, s[22:23]
	s_add_u32 s22, s22, 0x3000
	s_addc_u32 s23, s23, 0
	global_load_dword v88, v4, s[22:23]
	s_add_u32 s22, s22, 0x3000
	s_addc_u32 s23, s23, 0
	global_load_dword v90, v4, s[22:23]
	s_add_u32 s22, s22, 0x3000
	s_addc_u32 s23, s23, 0
	global_load_dword v92, v4, s[22:23]
	s_add_u32 s22, s22, 0x3000
	s_addc_u32 s23, s23, 0
	global_load_dword v94, v4, s[22:23]
	s_add_u32 s22, s22, 0x3000
	s_addc_u32 s23, s23, 0
	global_load_dword v96, v4, s[22:23]
	s_add_u32 s22, s22, 0x3000
	s_addc_u32 s23, s23, 0
	global_load_dword v98, v4, s[22:23]
	s_add_u32 s22, s22, 0x3000
	s_addc_u32 s23, s23, 0
	global_load_dword v100, v4, s[22:23]
	s_add_u32 s22, s22, 0x3000
	s_addc_u32 s23, s23, 0
	global_load_dword v102, v4, s[22:23]
	s_add_u32 s22, s22, 0x3000
	s_addc_u32 s23, s23, 0
.Lmod_loop:
	global_load_dword v104, v4, s[22:23]
	s_add_u32 s22, s22, 0x3000
	s_addc_u32 s23, s23, 0
	global_load_dword v106, v4, s[22:23]
	s_add_u32 s22, s22, 0x3000
	s_addc_u32 s23, s23, 0
	global_load_dword v108, v4, s[22:23]
	s_add_u32 s22, s22, 0x3000
	s_addc_u32 s23, s23, 0
	global_load_dword v110, v4, s[22:23]
	s_add_u32 s22, s22, 0x3000
	s_addc_u32 s23, s23, 0
	global_load_dword v112, v4, s[22:23]
	s_add_u32 s22, s22, 0x3000
	s_addc_u32 s23, s23, 0
	global_load_dword v114, v4, s[22:23]
	s_add_u32 s22, s22, 0x3000
	s_addc_u32 s23, s23, 0
	global_load_dword v116, v4, s[22:23]
	s_add_u32 s22, s22, 0x3000
	s_addc_u32 s23, s23, 0
	global_load_dword v118, v4, s[22:23]
	s_add_u32 s22, s22, 0x3000
	s_addc_u32 s23, s23, 0
	ds_read_b128 v[16:19], v15
	ds_read_b128 v[20:23], v15 offset:16
	ds_read_b128 v[24:27], v15 offset:4096
	ds_read_b128 v[28:31], v15 offset:4112
	ds_read_b128 v[32:35], v15 offset:8192
	ds_read_b128 v[36:39], v15 offset:8208
	ds_read_b128 v[40:43], v15 offset:12288
	ds_read_b128 v[44:47], v15 offset:12304
	s_waitcnt lgkmcnt(7)
	v_mov_b32_e32 v64, v16
	s_waitcnt lgkmcnt(5)
	v_mov_b32_e32 v65, v24
	s_waitcnt lgkmcnt(3)
	v_mov_b32_e32 v67, v32
	s_waitcnt lgkmcnt(1)
	v_mov_b32_e32 v66, v40
	v_mov_b32_e32 v24, v17
	v_mov_b32_e32 v32, v41
	v_mov_b32_e32 v16, v18
	v_mov_b32_e32 v17, v26
	v_mov_b32_e32 v40, v42
	v_mov_b32_e32 v41, v34
	v_mov_b32_e32 v26, v19
	v_mov_b32_e32 v34, v43
	v_mov_b32_e32 v18, v20
	v_mov_b32_e32 v19, v28
	s_waitcnt lgkmcnt(0)
	v_mov_b32_e32 v42, v44
	v_mov_b32_e32 v43, v36
	v_mov_b32_e32 v28, v21
	v_mov_b32_e32 v36, v45
	v_mov_b32_e32 v20, v22
	v_mov_b32_e32 v21, v30
	v_mov_b32_e32 v44, v46
	v_mov_b32_e32 v45, v38
	v_mov_b32_e32 v30, v23
	v_mov_b32_e32 v38, v47
	v_add_u32_e32 v15, 32, v15
	s_waitcnt vmcnt(31)
	v_pk_fma_f32 v[8:9], v[48:49], v[64:65], v[8:9] op_sel_hi:[0,1,1]
	v_pk_fma_f32 v[10:11], v[48:49], v[66:67], v[10:11] op_sel_hi:[0,1,1]
	s_waitcnt vmcnt(30)
	v_pk_fma_f32 v[8:9], v[50:51], v[24:25], v[8:9] op_sel_hi:[0,1,1]
	v_pk_fma_f32 v[10:11], v[50:51], v[32:33], v[10:11] op_sel_hi:[0,1,1]
	s_waitcnt vmcnt(29)
	v_pk_fma_f32 v[8:9], v[52:53], v[16:17], v[8:9] op_sel_hi:[0,1,1]
	v_pk_fma_f32 v[10:11], v[52:53], v[40:41], v[10:11] op_sel_hi:[0,1,1]
	s_waitcnt vmcnt(28)
	v_pk_fma_f32 v[8:9], v[54:55], v[26:27], v[8:9] op_sel_hi:[0,1,1]
	v_pk_fma_f32 v[10:11], v[54:55], v[34:35], v[10:11] op_sel_hi:[0,1,1]
	s_waitcnt vmcnt(27)
	v_pk_fma_f32 v[8:9], v[56:57], v[18:19], v[8:9] op_sel_hi:[0,1,1]
	v_pk_fma_f32 v[10:11], v[56:57], v[42:43], v[10:11] op_sel_hi:[0,1,1]
	s_waitcnt vmcnt(26)
	v_pk_fma_f32 v[8:9], v[58:59], v[28:29], v[8:9] op_sel_hi:[0,1,1]
	v_pk_fma_f32 v[10:11], v[58:59], v[36:37], v[10:11] op_sel_hi:[0,1,1]
	s_waitcnt vmcnt(25)
	v_pk_fma_f32 v[8:9], v[60:61], v[20:21], v[8:9] op_sel_hi:[0,1,1]
	v_pk_fma_f32 v[10:11], v[60:61], v[44:45], v[10:11] op_sel_hi:[0,1,1]
	s_waitcnt vmcnt(24)
	v_pk_fma_f32 v[8:9], v[62:63], v[30:31], v[8:9] op_sel_hi:[0,1,1]
	v_pk_fma_f32 v[10:11], v[62:63], v[38:39], v[10:11] op_sel_hi:[0,1,1]
	global_load_dword v48, v4, s[22:23]
	s_add_u32 s22, s22, 0x3000
	s_addc_u32 s23, s23, 0
	global_load_dword v50, v4, s[22:23]
	s_add_u32 s22, s22, 0x3000
	s_addc_u32 s23, s23, 0
	global_load_dword v52, v4, s[22:23]
	s_add_u32 s22, s22, 0x3000
	s_addc_u32 s23, s23, 0
	global_load_dword v54, v4, s[22:23]
	s_add_u32 s22, s22, 0x3000
	s_addc_u32 s23, s23, 0
	global_load_dword v56, v4, s[22:23]
	s_add_u32 s22, s22, 0x3000
	s_addc_u32 s23, s23, 0
	global_load_dword v58, v4, s[22:23]
	s_add_u32 s22, s22, 0x3000
	s_addc_u32 s23, s23, 0
	global_load_dword v60, v4, s[22:23]
	s_add_u32 s22, s22, 0x3000
	s_addc_u32 s23, s23, 0
	global_load_dword v62, v4, s[22:23]
	s_add_u32 s22, s22, 0x3000
	s_addc_u32 s23, s23, 0
	ds_read_b128 v[16:19], v15
	ds_read_b128 v[20:23], v15 offset:16
	ds_read_b128 v[24:27], v15 offset:4096
	ds_read_b128 v[28:31], v15 offset:4112
	ds_read_b128 v[32:35], v15 offset:8192
	ds_read_b128 v[36:39], v15 offset:8208
	ds_read_b128 v[40:43], v15 offset:12288
	ds_read_b128 v[44:47], v15 offset:12304
	s_waitcnt lgkmcnt(7)
	v_mov_b32_e32 v64, v16
	s_waitcnt lgkmcnt(5)
	v_mov_b32_e32 v65, v24
	s_waitcnt lgkmcnt(3)
	v_mov_b32_e32 v67, v32
	s_waitcnt lgkmcnt(1)
	v_mov_b32_e32 v66, v40
	v_mov_b32_e32 v24, v17
	v_mov_b32_e32 v32, v41
	v_mov_b32_e32 v16, v18
	v_mov_b32_e32 v17, v26
	v_mov_b32_e32 v40, v42
	v_mov_b32_e32 v41, v34
	v_mov_b32_e32 v26, v19
	v_mov_b32_e32 v34, v43
	v_mov_b32_e32 v18, v20
	v_mov_b32_e32 v19, v28
	s_waitcnt lgkmcnt(0)
	v_mov_b32_e32 v42, v44
	v_mov_b32_e32 v43, v36
	v_mov_b32_e32 v28, v21
	v_mov_b32_e32 v36, v45
	v_mov_b32_e32 v20, v22
	v_mov_b32_e32 v21, v30
	v_mov_b32_e32 v44, v46
	v_mov_b32_e32 v45, v38
	v_mov_b32_e32 v30, v23
	v_mov_b32_e32 v38, v47
	v_add_u32_e32 v15, 32, v15
	s_waitcnt vmcnt(31)
	v_pk_fma_f32 v[8:9], v[72:73], v[64:65], v[8:9] op_sel_hi:[0,1,1]
	v_pk_fma_f32 v[10:11], v[72:73], v[66:67], v[10:11] op_sel_hi:[0,1,1]
	s_waitcnt vmcnt(30)
	v_pk_fma_f32 v[8:9], v[74:75], v[24:25], v[8:9] op_sel_hi:[0,1,1]
	v_pk_fma_f32 v[10:11], v[74:75], v[32:33], v[10:11] op_sel_hi:[0,1,1]
	s_waitcnt vmcnt(29)
	v_pk_fma_f32 v[8:9], v[76:77], v[16:17], v[8:9] op_sel_hi:[0,1,1]
	v_pk_fma_f32 v[10:11], v[76:77], v[40:41], v[10:11] op_sel_hi:[0,1,1]
	s_waitcnt vmcnt(28)
	v_pk_fma_f32 v[8:9], v[78:79], v[26:27], v[8:9] op_sel_hi:[0,1,1]
	v_pk_fma_f32 v[10:11], v[78:79], v[34:35], v[10:11] op_sel_hi:[0,1,1]
	s_waitcnt vmcnt(27)
	v_pk_fma_f32 v[8:9], v[80:81], v[18:19], v[8:9] op_sel_hi:[0,1,1]
	v_pk_fma_f32 v[10:11], v[80:81], v[42:43], v[10:11] op_sel_hi:[0,1,1]
	s_waitcnt vmcnt(26)
	v_pk_fma_f32 v[8:9], v[82:83], v[28:29], v[8:9] op_sel_hi:[0,1,1]
	v_pk_fma_f32 v[10:11], v[82:83], v[36:37], v[10:11] op_sel_hi:[0,1,1]
	s_waitcnt vmcnt(25)
	v_pk_fma_f32 v[8:9], v[84:85], v[20:21], v[8:9] op_sel_hi:[0,1,1]
	v_pk_fma_f32 v[10:11], v[84:85], v[44:45], v[10:11] op_sel_hi:[0,1,1]
	s_waitcnt vmcnt(24)
	v_pk_fma_f32 v[8:9], v[86:87], v[30:31], v[8:9] op_sel_hi:[0,1,1]
	v_pk_fma_f32 v[10:11], v[86:87], v[38:39], v[10:11] op_sel_hi:[0,1,1]
	global_load_dword v72, v4, s[22:23]
	s_add_u32 s22, s22, 0x3000
	s_addc_u32 s23, s23, 0
	global_load_dword v74, v4, s[22:23]
	s_add_u32 s22, s22, 0x3000
	s_addc_u32 s23, s23, 0
	global_load_dword v76, v4, s[22:23]
	s_add_u32 s22, s22, 0x3000
	s_addc_u32 s23, s23, 0
	global_load_dword v78, v4, s[22:23]
	s_add_u32 s22, s22, 0x3000
	s_addc_u32 s23, s23, 0
	global_load_dword v80, v4, s[22:23]
	s_add_u32 s22, s22, 0x3000
	s_addc_u32 s23, s23, 0
	global_load_dword v82, v4, s[22:23]
	s_add_u32 s22, s22, 0x3000
	s_addc_u32 s23, s23, 0
	global_load_dword v84, v4, s[22:23]
	s_add_u32 s22, s22, 0x3000
	s_addc_u32 s23, s23, 0
	global_load_dword v86, v4, s[22:23]
	s_add_u32 s22, s22, 0x3000
	s_addc_u32 s23, s23, 0
	ds_read_b128 v[16:19], v15
	ds_read_b128 v[20:23], v15 offset:16
	ds_read_b128 v[24:27], v15 offset:4096
	ds_read_b128 v[28:31], v15 offset:4112
	ds_read_b128 v[32:35], v15 offset:8192
	ds_read_b128 v[36:39], v15 offset:8208
	ds_read_b128 v[40:43], v15 offset:12288
	ds_read_b128 v[44:47], v15 offset:12304
	s_waitcnt lgkmcnt(7)
	v_mov_b32_e32 v64, v16
	s_waitcnt lgkmcnt(5)
	v_mov_b32_e32 v65, v24
	s_waitcnt lgkmcnt(3)
	v_mov_b32_e32 v67, v32
	s_waitcnt lgkmcnt(1)
	v_mov_b32_e32 v66, v40
	v_mov_b32_e32 v24, v17
	v_mov_b32_e32 v32, v41
	v_mov_b32_e32 v16, v18
	v_mov_b32_e32 v17, v26
	v_mov_b32_e32 v40, v42
	v_mov_b32_e32 v41, v34
	v_mov_b32_e32 v26, v19
	v_mov_b32_e32 v34, v43
	v_mov_b32_e32 v18, v20
	v_mov_b32_e32 v19, v28
	s_waitcnt lgkmcnt(0)
	v_mov_b32_e32 v42, v44
	v_mov_b32_e32 v43, v36
	v_mov_b32_e32 v28, v21
	v_mov_b32_e32 v36, v45
	v_mov_b32_e32 v20, v22
	v_mov_b32_e32 v21, v30
	v_mov_b32_e32 v44, v46
	v_mov_b32_e32 v45, v38
	v_mov_b32_e32 v30, v23
	v_mov_b32_e32 v38, v47
	v_add_u32_e32 v15, 32, v15
	s_waitcnt vmcnt(31)
	v_pk_fma_f32 v[8:9], v[88:89], v[64:65], v[8:9] op_sel_hi:[0,1,1]
	v_pk_fma_f32 v[10:11], v[88:89], v[66:67], v[10:11] op_sel_hi:[0,1,1]
	s_waitcnt vmcnt(30)
	v_pk_fma_f32 v[8:9], v[90:91], v[24:25], v[8:9] op_sel_hi:[0,1,1]
	v_pk_fma_f32 v[10:11], v[90:91], v[32:33], v[10:11] op_sel_hi:[0,1,1]
	s_waitcnt vmcnt(29)
	v_pk_fma_f32 v[8:9], v[92:93], v[16:17], v[8:9] op_sel_hi:[0,1,1]
	v_pk_fma_f32 v[10:11], v[92:93], v[40:41], v[10:11] op_sel_hi:[0,1,1]
	s_waitcnt vmcnt(28)
	v_pk_fma_f32 v[8:9], v[94:95], v[26:27], v[8:9] op_sel_hi:[0,1,1]
	v_pk_fma_f32 v[10:11], v[94:95], v[34:35], v[10:11] op_sel_hi:[0,1,1]
	s_waitcnt vmcnt(27)
	v_pk_fma_f32 v[8:9], v[96:97], v[18:19], v[8:9] op_sel_hi:[0,1,1]
	v_pk_fma_f32 v[10:11], v[96:97], v[42:43], v[10:11] op_sel_hi:[0,1,1]
	s_waitcnt vmcnt(26)
	v_pk_fma_f32 v[8:9], v[98:99], v[28:29], v[8:9] op_sel_hi:[0,1,1]
	v_pk_fma_f32 v[10:11], v[98:99], v[36:37], v[10:11] op_sel_hi:[0,1,1]
	s_waitcnt vmcnt(25)
	v_pk_fma_f32 v[8:9], v[100:101], v[20:21], v[8:9] op_sel_hi:[0,1,1]
	v_pk_fma_f32 v[10:11], v[100:101], v[44:45], v[10:11] op_sel_hi:[0,1,1]
	s_waitcnt vmcnt(24)
	v_pk_fma_f32 v[8:9], v[102:103], v[30:31], v[8:9] op_sel_hi:[0,1,1]
	v_pk_fma_f32 v[10:11], v[102:103], v[38:39], v[10:11] op_sel_hi:[0,1,1]
	global_load_dword v88, v4, s[22:23]
	s_add_u32 s22, s22, 0x3000
	s_addc_u32 s23, s23, 0
	global_load_dword v90, v4, s[22:23]
	s_add_u32 s22, s22, 0x3000
	s_addc_u32 s23, s23, 0
	global_load_dword v92, v4, s[22:23]
	s_add_u32 s22, s22, 0x3000
	s_addc_u32 s23, s23, 0
	global_load_dword v94, v4, s[22:23]
	s_add_u32 s22, s22, 0x3000
	s_addc_u32 s23, s23, 0
	global_load_dword v96, v4, s[22:23]
	s_add_u32 s22, s22, 0x3000
	s_addc_u32 s23, s23, 0
	global_load_dword v98, v4, s[22:23]
	s_add_u32 s22, s22, 0x3000
	s_addc_u32 s23, s23, 0
	global_load_dword v100, v4, s[22:23]
	s_add_u32 s22, s22, 0x3000
	s_addc_u32 s23, s23, 0
	global_load_dword v102, v4, s[22:23]
	s_add_u32 s22, s22, 0x3000
	s_addc_u32 s23, s23, 0
	ds_read_b128 v[16:19], v15
	ds_read_b128 v[20:23], v15 offset:16
	ds_read_b128 v[24:27], v15 offset:4096
	ds_read_b128 v[28:31], v15 offset:4112
	ds_read_b128 v[32:35], v15 offset:8192
	ds_read_b128 v[36:39], v15 offset:8208
	ds_read_b128 v[40:43], v15 offset:12288
	ds_read_b128 v[44:47], v15 offset:12304
	s_waitcnt lgkmcnt(7)
	v_mov_b32_e32 v64, v16
	s_waitcnt lgkmcnt(5)
	v_mov_b32_e32 v65, v24
	s_waitcnt lgkmcnt(3)
	v_mov_b32_e32 v67, v32
	s_waitcnt lgkmcnt(1)
	v_mov_b32_e32 v66, v40
	v_mov_b32_e32 v24, v17
	v_mov_b32_e32 v32, v41
	v_mov_b32_e32 v16, v18
	v_mov_b32_e32 v17, v26
	v_mov_b32_e32 v40, v42
	v_mov_b32_e32 v41, v34
	v_mov_b32_e32 v26, v19
	v_mov_b32_e32 v34, v43
	v_mov_b32_e32 v18, v20
	v_mov_b32_e32 v19, v28
	s_waitcnt lgkmcnt(0)
	v_mov_b32_e32 v42, v44
	v_mov_b32_e32 v43, v36
	v_mov_b32_e32 v28, v21
	v_mov_b32_e32 v36, v45
	v_mov_b32_e32 v20, v22
	v_mov_b32_e32 v21, v30
	v_mov_b32_e32 v44, v46
	v_mov_b32_e32 v45, v38
	v_mov_b32_e32 v30, v23
	v_mov_b32_e32 v38, v47
	v_add_u32_e32 v15, 32, v15
	s_waitcnt vmcnt(31)
	v_pk_fma_f32 v[8:9], v[104:105], v[64:65], v[8:9] op_sel_hi:[0,1,1]
	v_pk_fma_f32 v[10:11], v[104:105], v[66:67], v[10:11] op_sel_hi:[0,1,1]
	s_waitcnt vmcnt(30)
	v_pk_fma_f32 v[8:9], v[106:107], v[24:25], v[8:9] op_sel_hi:[0,1,1]
	v_pk_fma_f32 v[10:11], v[106:107], v[32:33], v[10:11] op_sel_hi:[0,1,1]
	s_waitcnt vmcnt(29)
	v_pk_fma_f32 v[8:9], v[108:109], v[16:17], v[8:9] op_sel_hi:[0,1,1]
	v_pk_fma_f32 v[10:11], v[108:109], v[40:41], v[10:11] op_sel_hi:[0,1,1]
	s_waitcnt vmcnt(28)
	v_pk_fma_f32 v[8:9], v[110:111], v[26:27], v[8:9] op_sel_hi:[0,1,1]
	v_pk_fma_f32 v[10:11], v[110:111], v[34:35], v[10:11] op_sel_hi:[0,1,1]
	s_waitcnt vmcnt(27)
	v_pk_fma_f32 v[8:9], v[112:113], v[18:19], v[8:9] op_sel_hi:[0,1,1]
	v_pk_fma_f32 v[10:11], v[112:113], v[42:43], v[10:11] op_sel_hi:[0,1,1]
	s_waitcnt vmcnt(26)
	v_pk_fma_f32 v[8:9], v[114:115], v[28:29], v[8:9] op_sel_hi:[0,1,1]
	v_pk_fma_f32 v[10:11], v[114:115], v[36:37], v[10:11] op_sel_hi:[0,1,1]
	s_waitcnt vmcnt(25)
	v_pk_fma_f32 v[8:9], v[116:117], v[20:21], v[8:9] op_sel_hi:[0,1,1]
	v_pk_fma_f32 v[10:11], v[116:117], v[44:45], v[10:11] op_sel_hi:[0,1,1]
	s_waitcnt vmcnt(24)
	v_pk_fma_f32 v[8:9], v[118:119], v[30:31], v[8:9] op_sel_hi:[0,1,1]
	v_pk_fma_f32 v[10:11], v[118:119], v[38:39], v[10:11] op_sel_hi:[0,1,1]
	s_add_i32 s24, s24, 1
	s_cmp_lt_u32 s24, 3
	s_cbranch_scc1 .Lmod_loop
	global_load_dword v104, v4, s[22:23]
	s_add_u32 s22, s22, 0x3000
	s_addc_u32 s23, s23, 0
	global_load_dword v106, v4, s[22:23]
	s_add_u32 s22, s22, 0x3000
	s_addc_u32 s23, s23, 0
	global_load_dword v108, v4, s[22:23]
	s_add_u32 s22, s22, 0x3000
	s_addc_u32 s23, s23, 0
	global_load_dword v110, v4, s[22:23]
	s_add_u32 s22, s22, 0x3000
	s_addc_u32 s23, s23, 0
	global_load_dword v112, v4, s[22:23]
	s_add_u32 s22, s22, 0x3000
	s_addc_u32 s23, s23, 0
	global_load_dword v114, v4, s[22:23]
	s_add_u32 s22, s22, 0x3000
	s_addc_u32 s23, s23, 0
	global_load_dword v116, v4, s[22:23]
	s_add_u32 s22, s22, 0x3000
	s_addc_u32 s23, s23, 0
	global_load_dword v118, v4, s[22:23]
	s_add_u32 s22, s22, 0x3000
	s_addc_u32 s23, s23, 0
	ds_read_b128 v[16:19], v15
	ds_read_b128 v[20:23], v15 offset:16
	ds_read_b128 v[24:27], v15 offset:4096
	ds_read_b128 v[28:31], v15 offset:4112
	ds_read_b128 v[32:35], v15 offset:8192
	ds_read_b128 v[36:39], v15 offset:8208
	ds_read_b128 v[40:43], v15 offset:12288
	ds_read_b128 v[44:47], v15 offset:12304
	s_waitcnt lgkmcnt(7)
	v_mov_b32_e32 v64, v16
	s_waitcnt lgkmcnt(5)
	v_mov_b32_e32 v65, v24
	s_waitcnt lgkmcnt(3)
	v_mov_b32_e32 v67, v32
	s_waitcnt lgkmcnt(1)
	v_mov_b32_e32 v66, v40
	v_mov_b32_e32 v24, v17
	v_mov_b32_e32 v32, v41
	v_mov_b32_e32 v16, v18
	v_mov_b32_e32 v17, v26
	v_mov_b32_e32 v40, v42
	v_mov_b32_e32 v41, v34
	v_mov_b32_e32 v26, v19
	v_mov_b32_e32 v34, v43
	v_mov_b32_e32 v18, v20
	v_mov_b32_e32 v19, v28
	s_waitcnt lgkmcnt(0)
	v_mov_b32_e32 v42, v44
	v_mov_b32_e32 v43, v36
	v_mov_b32_e32 v28, v21
	v_mov_b32_e32 v36, v45
	v_mov_b32_e32 v20, v22
	v_mov_b32_e32 v21, v30
	v_mov_b32_e32 v44, v46
	v_mov_b32_e32 v45, v38
	v_mov_b32_e32 v30, v23
	v_mov_b32_e32 v38, v47
	v_add_u32_e32 v15, 32, v15
	s_waitcnt vmcnt(31)
	v_pk_fma_f32 v[8:9], v[48:49], v[64:65], v[8:9] op_sel_hi:[0,1,1]
	v_pk_fma_f32 v[10:11], v[48:49], v[66:67], v[10:11] op_sel_hi:[0,1,1]
	s_waitcnt vmcnt(30)
	v_pk_fma_f32 v[8:9], v[50:51], v[24:25], v[8:9] op_sel_hi:[0,1,1]
	v_pk_fma_f32 v[10:11], v[50:51], v[32:33], v[10:11] op_sel_hi:[0,1,1]
	s_waitcnt vmcnt(29)
	v_pk_fma_f32 v[8:9], v[52:53], v[16:17], v[8:9] op_sel_hi:[0,1,1]
	v_pk_fma_f32 v[10:11], v[52:53], v[40:41], v[10:11] op_sel_hi:[0,1,1]
	s_waitcnt vmcnt(28)
	v_pk_fma_f32 v[8:9], v[54:55], v[26:27], v[8:9] op_sel_hi:[0,1,1]
	v_pk_fma_f32 v[10:11], v[54:55], v[34:35], v[10:11] op_sel_hi:[0,1,1]
	s_waitcnt vmcnt(27)
	v_pk_fma_f32 v[8:9], v[56:57], v[18:19], v[8:9] op_sel_hi:[0,1,1]
	v_pk_fma_f32 v[10:11], v[56:57], v[42:43], v[10:11] op_sel_hi:[0,1,1]
	s_waitcnt vmcnt(26)
	v_pk_fma_f32 v[8:9], v[58:59], v[28:29], v[8:9] op_sel_hi:[0,1,1]
	v_pk_fma_f32 v[10:11], v[58:59], v[36:37], v[10:11] op_sel_hi:[0,1,1]
	s_waitcnt vmcnt(25)
	v_pk_fma_f32 v[8:9], v[60:61], v[20:21], v[8:9] op_sel_hi:[0,1,1]
	v_pk_fma_f32 v[10:11], v[60:61], v[44:45], v[10:11] op_sel_hi:[0,1,1]
	s_waitcnt vmcnt(24)
	v_pk_fma_f32 v[8:9], v[62:63], v[30:31], v[8:9] op_sel_hi:[0,1,1]
	v_pk_fma_f32 v[10:11], v[62:63], v[38:39], v[10:11] op_sel_hi:[0,1,1]
	ds_read_b128 v[16:19], v15
	ds_read_b128 v[20:23], v15 offset:16
	ds_read_b128 v[24:27], v15 offset:4096
	ds_read_b128 v[28:31], v15 offset:4112
	ds_read_b128 v[32:35], v15 offset:8192
	ds_read_b128 v[36:39], v15 offset:8208
	ds_read_b128 v[40:43], v15 offset:12288
	ds_read_b128 v[44:47], v15 offset:12304
	s_waitcnt lgkmcnt(7)
	v_mov_b32_e32 v64, v16
	s_waitcnt lgkmcnt(5)
	v_mov_b32_e32 v65, v24
	s_waitcnt lgkmcnt(3)
	v_mov_b32_e32 v67, v32
	s_waitcnt lgkmcnt(1)
	v_mov_b32_e32 v66, v40
	v_mov_b32_e32 v24, v17
	v_mov_b32_e32 v32, v41
	v_mov_b32_e32 v16, v18
	v_mov_b32_e32 v17, v26
	v_mov_b32_e32 v40, v42
	v_mov_b32_e32 v41, v34
	v_mov_b32_e32 v26, v19
	v_mov_b32_e32 v34, v43
	v_mov_b32_e32 v18, v20
	v_mov_b32_e32 v19, v28
	s_waitcnt lgkmcnt(0)
	v_mov_b32_e32 v42, v44
	v_mov_b32_e32 v43, v36
	v_mov_b32_e32 v28, v21
	v_mov_b32_e32 v36, v45
	v_mov_b32_e32 v20, v22
	v_mov_b32_e32 v21, v30
	v_mov_b32_e32 v44, v46
	v_mov_b32_e32 v45, v38
	v_mov_b32_e32 v30, v23
	v_mov_b32_e32 v38, v47
	v_add_u32_e32 v15, 32, v15
	s_waitcnt vmcnt(23)
	v_pk_fma_f32 v[8:9], v[72:73], v[64:65], v[8:9] op_sel_hi:[0,1,1]
	v_pk_fma_f32 v[10:11], v[72:73], v[66:67], v[10:11] op_sel_hi:[0,1,1]
	s_waitcnt vmcnt(22)
	v_pk_fma_f32 v[8:9], v[74:75], v[24:25], v[8:9] op_sel_hi:[0,1,1]
	v_pk_fma_f32 v[10:11], v[74:75], v[32:33], v[10:11] op_sel_hi:[0,1,1]
	s_waitcnt vmcnt(21)
	v_pk_fma_f32 v[8:9], v[76:77], v[16:17], v[8:9] op_sel_hi:[0,1,1]
	v_pk_fma_f32 v[10:11], v[76:77], v[40:41], v[10:11] op_sel_hi:[0,1,1]
	s_waitcnt vmcnt(20)
	v_pk_fma_f32 v[8:9], v[78:79], v[26:27], v[8:9] op_sel_hi:[0,1,1]
	v_pk_fma_f32 v[10:11], v[78:79], v[34:35], v[10:11] op_sel_hi:[0,1,1]
	s_waitcnt vmcnt(19)
	v_pk_fma_f32 v[8:9], v[80:81], v[18:19], v[8:9] op_sel_hi:[0,1,1]
	v_pk_fma_f32 v[10:11], v[80:81], v[42:43], v[10:11] op_sel_hi:[0,1,1]
	s_waitcnt vmcnt(18)
	v_pk_fma_f32 v[8:9], v[82:83], v[28:29], v[8:9] op_sel_hi:[0,1,1]
	v_pk_fma_f32 v[10:11], v[82:83], v[36:37], v[10:11] op_sel_hi:[0,1,1]
	s_waitcnt vmcnt(17)
	v_pk_fma_f32 v[8:9], v[84:85], v[20:21], v[8:9] op_sel_hi:[0,1,1]
	v_pk_fma_f32 v[10:11], v[84:85], v[44:45], v[10:11] op_sel_hi:[0,1,1]
	s_waitcnt vmcnt(16)
	v_pk_fma_f32 v[8:9], v[86:87], v[30:31], v[8:9] op_sel_hi:[0,1,1]
	v_pk_fma_f32 v[10:11], v[86:87], v[38:39], v[10:11] op_sel_hi:[0,1,1]
	ds_read_b128 v[16:19], v15
	ds_read_b128 v[20:23], v15 offset:16
	ds_read_b128 v[24:27], v15 offset:4096
	ds_read_b128 v[28:31], v15 offset:4112
	ds_read_b128 v[32:35], v15 offset:8192
	ds_read_b128 v[36:39], v15 offset:8208
	ds_read_b128 v[40:43], v15 offset:12288
	ds_read_b128 v[44:47], v15 offset:12304
	s_waitcnt lgkmcnt(7)
	v_mov_b32_e32 v64, v16
	s_waitcnt lgkmcnt(5)
	v_mov_b32_e32 v65, v24
	s_waitcnt lgkmcnt(3)
	v_mov_b32_e32 v67, v32
	s_waitcnt lgkmcnt(1)
	v_mov_b32_e32 v66, v40
	v_mov_b32_e32 v24, v17
	v_mov_b32_e32 v32, v41
	v_mov_b32_e32 v16, v18
	v_mov_b32_e32 v17, v26
	v_mov_b32_e32 v40, v42
	v_mov_b32_e32 v41, v34
	v_mov_b32_e32 v26, v19
	v_mov_b32_e32 v34, v43
	v_mov_b32_e32 v18, v20
	v_mov_b32_e32 v19, v28
	s_waitcnt lgkmcnt(0)
	v_mov_b32_e32 v42, v44
	v_mov_b32_e32 v43, v36
	v_mov_b32_e32 v28, v21
	v_mov_b32_e32 v36, v45
	v_mov_b32_e32 v20, v22
	v_mov_b32_e32 v21, v30
	v_mov_b32_e32 v44, v46
	v_mov_b32_e32 v45, v38
	v_mov_b32_e32 v30, v23
	v_mov_b32_e32 v38, v47
	v_add_u32_e32 v15, 32, v15
	s_waitcnt vmcnt(15)
	v_pk_fma_f32 v[8:9], v[88:89], v[64:65], v[8:9] op_sel_hi:[0,1,1]
	v_pk_fma_f32 v[10:11], v[88:89], v[66:67], v[10:11] op_sel_hi:[0,1,1]
	s_waitcnt vmcnt(14)
	v_pk_fma_f32 v[8:9], v[90:91], v[24:25], v[8:9] op_sel_hi:[0,1,1]
	v_pk_fma_f32 v[10:11], v[90:91], v[32:33], v[10:11] op_sel_hi:[0,1,1]
	s_waitcnt vmcnt(13)
	v_pk_fma_f32 v[8:9], v[92:93], v[16:17], v[8:9] op_sel_hi:[0,1,1]
	v_pk_fma_f32 v[10:11], v[92:93], v[40:41], v[10:11] op_sel_hi:[0,1,1]
	s_waitcnt vmcnt(12)
	v_pk_fma_f32 v[8:9], v[94:95], v[26:27], v[8:9] op_sel_hi:[0,1,1]
	v_pk_fma_f32 v[10:11], v[94:95], v[34:35], v[10:11] op_sel_hi:[0,1,1]
	s_waitcnt vmcnt(11)
	v_pk_fma_f32 v[8:9], v[96:97], v[18:19], v[8:9] op_sel_hi:[0,1,1]
	v_pk_fma_f32 v[10:11], v[96:97], v[42:43], v[10:11] op_sel_hi:[0,1,1]
	s_waitcnt vmcnt(10)
	v_pk_fma_f32 v[8:9], v[98:99], v[28:29], v[8:9] op_sel_hi:[0,1,1]
	v_pk_fma_f32 v[10:11], v[98:99], v[36:37], v[10:11] op_sel_hi:[0,1,1]
	s_waitcnt vmcnt(9)
	v_pk_fma_f32 v[8:9], v[100:101], v[20:21], v[8:9] op_sel_hi:[0,1,1]
	v_pk_fma_f32 v[10:11], v[100:101], v[44:45], v[10:11] op_sel_hi:[0,1,1]
	s_waitcnt vmcnt(8)
	v_pk_fma_f32 v[8:9], v[102:103], v[30:31], v[8:9] op_sel_hi:[0,1,1]
	v_pk_fma_f32 v[10:11], v[102:103], v[38:39], v[10:11] op_sel_hi:[0,1,1]
	ds_read_b128 v[16:19], v15
	ds_read_b128 v[20:23], v15 offset:16
	ds_read_b128 v[24:27], v15 offset:4096
	ds_read_b128 v[28:31], v15 offset:4112
	ds_read_b128 v[32:35], v15 offset:8192
	ds_read_b128 v[36:39], v15 offset:8208
	ds_read_b128 v[40:43], v15 offset:12288
	ds_read_b128 v[44:47], v15 offset:12304
	s_waitcnt lgkmcnt(7)
	v_mov_b32_e32 v64, v16
	s_waitcnt lgkmcnt(5)
	v_mov_b32_e32 v65, v24
	s_waitcnt lgkmcnt(3)
	v_mov_b32_e32 v67, v32
	s_waitcnt lgkmcnt(1)
	v_mov_b32_e32 v66, v40
	v_mov_b32_e32 v24, v17
	v_mov_b32_e32 v32, v41
	v_mov_b32_e32 v16, v18
	v_mov_b32_e32 v17, v26
	v_mov_b32_e32 v40, v42
	v_mov_b32_e32 v41, v34
	v_mov_b32_e32 v26, v19
	v_mov_b32_e32 v34, v43
	v_mov_b32_e32 v18, v20
	v_mov_b32_e32 v19, v28
	s_waitcnt lgkmcnt(0)
	v_mov_b32_e32 v42, v44
	v_mov_b32_e32 v43, v36
	v_mov_b32_e32 v28, v21
	v_mov_b32_e32 v36, v45
	v_mov_b32_e32 v20, v22
	v_mov_b32_e32 v21, v30
	v_mov_b32_e32 v44, v46
	v_mov_b32_e32 v45, v38
	v_mov_b32_e32 v30, v23
	v_mov_b32_e32 v38, v47
	v_add_u32_e32 v15, 32, v15
	s_waitcnt vmcnt(7)
	v_pk_fma_f32 v[8:9], v[104:105], v[64:65], v[8:9] op_sel_hi:[0,1,1]
	v_pk_fma_f32 v[10:11], v[104:105], v[66:67], v[10:11] op_sel_hi:[0,1,1]
	s_waitcnt vmcnt(6)
	v_pk_fma_f32 v[8:9], v[106:107], v[24:25], v[8:9] op_sel_hi:[0,1,1]
	v_pk_fma_f32 v[10:11], v[106:107], v[32:33], v[10:11] op_sel_hi:[0,1,1]
	s_waitcnt vmcnt(5)
	v_pk_fma_f32 v[8:9], v[108:109], v[16:17], v[8:9] op_sel_hi:[0,1,1]
	v_pk_fma_f32 v[10:11], v[108:109], v[40:41], v[10:11] op_sel_hi:[0,1,1]
	s_waitcnt vmcnt(4)
	v_pk_fma_f32 v[8:9], v[110:111], v[26:27], v[8:9] op_sel_hi:[0,1,1]
	v_pk_fma_f32 v[10:11], v[110:111], v[34:35], v[10:11] op_sel_hi:[0,1,1]
	s_waitcnt vmcnt(3)
	v_pk_fma_f32 v[8:9], v[112:113], v[18:19], v[8:9] op_sel_hi:[0,1,1]
	v_pk_fma_f32 v[10:11], v[112:113], v[42:43], v[10:11] op_sel_hi:[0,1,1]
	s_waitcnt vmcnt(2)
	v_pk_fma_f32 v[8:9], v[114:115], v[28:29], v[8:9] op_sel_hi:[0,1,1]
	v_pk_fma_f32 v[10:11], v[114:115], v[36:37], v[10:11] op_sel_hi:[0,1,1]
	s_waitcnt vmcnt(1)
	v_pk_fma_f32 v[8:9], v[116:117], v[20:21], v[8:9] op_sel_hi:[0,1,1]
	v_pk_fma_f32 v[10:11], v[116:117], v[44:45], v[10:11] op_sel_hi:[0,1,1]
	s_waitcnt vmcnt(0)
	v_pk_fma_f32 v[8:9], v[118:119], v[30:31], v[8:9] op_sel_hi:[0,1,1]
	v_pk_fma_f32 v[10:11], v[118:119], v[38:39], v[10:11] op_sel_hi:[0,1,1]
	ds_write2st64_b32 v14, v8, v9 offset0:64 offset1:65
	ds_write2st64_b32 v14, v11, v10 offset0:66 offset1:67
	s_waitcnt lgkmcnt(0)
	s_barrier
	s_and_saveexec_b64 s[6:7], vcc
	s_cbranch_execz .LBB0_100
	v_or_b32_e32 v15, s4, v2
	s_mul_i32 s8, s18, 0xc00
	v_readlane_b32 s4, v254, 1
	v_add_u32_e32 v18, s8, v15
	v_readlane_b32 s5, v254, 2
	v_ashrrev_i32_e32 v19, 31, v18
	ds_read2st64_b32 v[6:7], v3 offset0:64 offset1:68
	ds_read2st64_b32 v[8:9], v3 offset0:72 offset1:76
	ds_read2st64_b32 v[10:11], v3 offset0:80 offset1:84
	ds_read2st64_b32 v[16:17], v3 offset0:88 offset1:92
	s_load_dwordx2 s[4:5], s[4:5], 0x80
	s_waitcnt lgkmcnt(0)
	s_waitcnt lgkmcnt(3)
	v_add_f32_e32 v6, 0, v6
	v_lshl_add_u64 v[18:19], v[18:19], 2, s[4:5]
	global_load_dword v19, v[18:19], off
	v_add_f32_e32 v6, v6, v7
	s_lshr_b32 s8, s19, 4
	s_waitcnt lgkmcnt(2)
	v_add_f32_e32 v6, v6, v8
	s_mul_i32 s9, s18, 3
	s_cmp_lt_u32 s19, 16
	v_add_f32_e32 v6, v6, v9
	s_cselect_b64 s[4:5], -1, 0
	s_add_i32 s9, s9, s8
	s_waitcnt lgkmcnt(1)
	v_add_f32_e32 v6, v6, v10
	v_lshl_add_u32 v18, s9, 12, v12
	v_add_f32_e32 v6, v6, v11
	v_cndmask_b32_e64 v21, 1.0, 0, s[4:5]
	v_and_or_b32 v22, v15, s16, v18
	s_waitcnt lgkmcnt(0)
	v_mov_b32_e32 v18, v17
	v_add_f32_e32 v20, v6, v16
	v_ashrrev_i32_e32 v23, 31, v22
	s_waitcnt vmcnt(0)
	v_pk_add_f32 v[6:7], v[20:21], v[18:19]
	s_nop 0
	v_add_f32_e32 v8, v6, v7
	v_lshl_add_u64 v[6:7], v[22:23], 2, s[0:1]
	global_store_dword v[6:7], v8, off
	s_branch .LBB0_100
